# baseline (speedup 1.0000x reference)
.LBB2_116:
	s_waitcnt vmcnt(0)
	v_and_b32_e32 v115, 15, v110
	v_lshlrev_b32_e32 v122, 4, v110
	v_mov_b32_e32 v23, 0
	v_mov_b32_e32 v123, v23
	v_or_b32_e32 v0, s33, v115
	v_lshl_add_u64 v[20:21], s[16:17], 0, v[122:123]
	s_mov_b32 s0, 0x4d000
	v_ashrrev_i32_e32 v1, 31, v0
	v_add_co_u32_e32 v36, vcc, s0, v20
	v_lshlrev_b64 v[0:1], 7, v[0:1]
	s_nop 0
	v_addc_co_u32_e32 v37, vcc, 0, v21, vcc
	s_mov_b32 s0, 0x4c000
	v_lshl_add_u64 v[4:5], s[28:29], 0, v[0:1]
	v_lshlrev_b32_e32 v22, 3, v107
	v_add_co_u32_e32 v54, vcc, s0, v20
	v_lshl_add_u64 v[12:13], v[4:5], 0, v[22:23]
	s_nop 0
	v_addc_co_u32_e32 v55, vcc, 0, v21, vcc
	global_load_dwordx4 v[0:3], v[36:37], off offset:-4096
	global_load_dwordx2 v[4:5], v[12:13], off
	global_load_dwordx2 v[6:7], v[12:13], off offset:32
	global_load_dwordx4 v[8:11], v[36:37], off
	global_load_dwordx2 v[24:25], v[12:13], off offset:64
	global_load_dwordx2 v[26:27], v[12:13], off offset:96
	v_lshlrev_b32_e32 v22, 4, v107
	global_load_dwordx4 v[12:15], v[54:55], off offset:2048
	s_mov_b32 s0, 0x3f200000
	s_waitcnt vmcnt(3)
	v_mfma_f32_16x16x32_f16 v[28:31], v[8:11], v[4:7], v[42:45]
	global_load_dwordx4 v[8:11], v[54:55], off offset:1024
	s_waitcnt vmcnt(1)
	v_mfma_f32_16x16x32_f16 v[16:19], v[12:15], v[4:7], v[46:49]
	global_load_dwordx4 v[12:15], v[36:37], off offset:2048
	v_mfma_f32_16x16x32_f16 v[0:3], v[0:3], v[4:7], v[50:53]
	s_waitcnt vmcnt(0)
	v_mfma_f32_16x16x32_f16 v[32:35], v[12:15], v[4:7], v[38:41]
	global_load_dwordx4 v[4:7], v[54:55], off offset:3072
	v_mfma_f32_16x16x32_f16 v[12:15], v[8:11], v[24:27], v[0:3]
	s_nop 3
	global_load_dwordx4 v[0:3], v[36:37], off offset:1024
	s_waitcnt vmcnt(1)
	v_mfma_f32_16x16x32_f16 v[8:11], v[4:7], v[24:27], v[16:19]
	global_load_dwordx4 v[36:39], v[36:37], off offset:3072
	s_nop 1
	global_load_dwordx4 v[16:19], v22, s[18:19]
	global_load_dwordx4 v[200:203], v22, s[18:19] offset:64
	global_load_dwordx4 v[204:207], v22, s[18:19] offset:128
	global_load_dwordx4 v[208:211], v22, s[18:19] offset:192
	global_load_dwordx4 v[184:187], v22, s[14:15]
	global_load_dwordx4 v[188:191], v22, s[14:15] offset:64
	global_load_dwordx4 v[192:195], v22, s[14:15] offset:128
	global_load_dwordx4 v[196:199], v22, s[14:15] offset:192
	v_lshlrev_b32_e32 v244, 4, v110
	v_mov_b32_e32 v245, 0
	s_mov_b32 s92, 0x4e000
	s_mov_b32 s93, 0
	v_lshl_add_u64 v[244:245], s[16:17], 0, v[244:245]
	s_mov_b32 s94, 0x1000
	s_mov_b32 s95, 0
	v_lshl_add_u64 v[244:245], v[244:245], 0, s[92:93]
	v_lshl_add_u64 v[246:247], v[244:245], 0, s[94:95]
	global_load_dwordx4 v[212:215], v[244:245], off
	global_load_dwordx4 v[216:219], v[244:245], off offset:1024
	global_load_dwordx4 v[220:223], v[244:245], off offset:2048
	global_load_dwordx4 v[224:227], v[244:245], off offset:3072
	global_load_dwordx4 v[228:231], v[246:247], off
	global_load_dwordx4 v[232:235], v[246:247], off offset:1024
	global_load_dwordx4 v[236:239], v[246:247], off offset:2048
	global_load_dwordx4 v[240:243], v[246:247], off offset:3072
	s_waitcnt vmcnt(17)
	v_mfma_f32_16x16x32_f16 v[4:7], v[0:3], v[24:27], v[28:31]
	s_waitcnt vmcnt(16)
	v_mfma_f32_16x16x32_f16 v[0:3], v[36:39], v[24:27], v[32:35]
	s_waitcnt vmcnt(0)
	v_add_f32_e32 v24, v12, v16
	v_cmp_nlt_f32_e64 s[0:1], |v24|, s0
	s_and_saveexec_b64 s[2:3], s[0:1]
	s_xor_b64 s[0:1], exec, s[2:3]
	s_cbranch_execz .LBB2_118
	v_add_f32_e64 v12, |v24|, |v24|
	v_mul_f32_e32 v16, 0x3fb8aa3b, v12
	s_mov_b32 s2, 0x3fb8aa3b
	v_rndne_f32_e32 v25, v16
	v_sub_f32_e32 v26, v16, v25
	v_fma_f32 v16, v12, s2, -v16
	v_fmamk_f32 v16, v12, 0x32a5705f, v16
	v_add_f32_e32 v16, v26, v16
	v_exp_f32_e32 v16, v16
	v_cvt_i32_f32_e32 v25, v25
	s_mov_b32 s2, 0xc2ce8ed0
	v_cmp_ngt_f32_e32 vcc, s2, v12
	s_mov_b32 s2, 0x42b17218
	v_ldexp_f32 v16, v16, v25
	v_cndmask_b32_e32 v16, 0, v16, vcc
	v_mov_b32_e32 v25, 0x7f800000
	v_cmp_nlt_f32_e32 vcc, s2, v12
	s_nop 1
	v_cndmask_b32_e32 v12, v25, v16, vcc
	v_add_f32_e32 v12, 1.0, v12
	v_rcp_f32_e32 v12, v12
	s_nop 0
	v_fma_f32 v25, v12, -2.0, 1.0

.LBB2_178:
	s_andn2_saveexec_b64 s[0:1], s[0:1]
	v_mul_f32_e32 v7, v3, v3
	v_mov_b32_e32 v17, 0x3ca908c9
	v_fmac_f32_e32 v17, 0xbbbac73d, v7
	v_fmaak_f32 v17, v7, v17, 0xbd5c1c4e
	v_fmaak_f32 v17, v7, v17, 0x3e088382
	v_fmaak_f32 v17, v7, v17, 0xbeaaaa99
	v_mul_f32_e64 v17, |v3|, v17
	v_fma_f32 v7, v7, v17, |v3|
	s_or_b64 exec, exec, s[0:1]
	s_mov_b32 s1, 0x4f000
	v_add_co_u32_e32 v64, vcc, s1, v20
	s_mov_b32 s0, 0x4e000
	s_nop 0
	v_addc_co_u32_e32 v65, vcc, 0, v21, vcc
	s_nop 0
	v_add_co_u32_e32 v20, vcc, s0, v20
	v_cvt_f16_f32_e32 v17, v32
	s_nop 0
	v_addc_co_u32_e32 v21, vcc, 0, v21, vcc
	s_nop 0
	s_nop 0
	s_nop 0
	s_nop 0
	s_nop 0
	s_nop 0
	v_cvt_f16_f32_e32 v21, v33
	v_lshrrev_b32_e32 v32, 16, v9
	v_cvt_f16_f32_e32 v33, v34
	v_lshrrev_b32_e32 v34, 16, v10
	v_lshrrev_b32_e32 v66, 16, v11
	v_lshrrev_b32_e32 v67, 16, v0
	v_lshrrev_b32_e32 v68, 16, v1
	v_lshrrev_b32_e32 v69, 16, v2
	v_cvt_f16_f32_e32 v0, v25
	v_lshrrev_b32_e32 v1, 16, v24
	v_cvt_f16_f32_e32 v2, v27
	v_cvt_f16_f32_e32 v9, v28
	v_lshrrev_b32_e32 v10, 16, v18
	v_cvt_f16_f32_e32 v11, v29
	v_lshrrev_b32_e32 v18, 16, v19
	v_cvt_f16_f32_e32 v19, v22
	v_cvt_f16_f32_e32 v22, v23
	v_cvt_f16_f32_e32 v23, v30
	v_cvt_f16_f32_e32 v24, v31
	v_cvt_f16_f32_e32 v35, v35
	v_cvt_f16_f32_e32 v4, v4
	v_cvt_f16_f32_e32 v5, v5
	v_cvt_f16_f32_e32 v7, v7
	v_lshrrev_b32_e32 v20, 16, v8
	s_movk_i32 s0, 0x7fff
	v_lshrrev_b32_e32 v8, 16, v26
	v_lshrrev_b32_e32 v12, 16, v12
	v_lshrrev_b32_e32 v13, 16, v13
	v_lshrrev_b32_e32 v14, 16, v14
	v_lshrrev_b32_e32 v15, 16, v15
	v_lshrrev_b32_e32 v25, 16, v3
	v_bfi_b32 v0, s0, v0, v1
	v_bfi_b32 v8, s0, v2, v8
	v_bfi_b32 v1, s0, v9, v10
	v_bfi_b32 v9, s0, v11, v18
	v_bfi_b32 v2, s0, v19, v12
	v_bfi_b32 v10, s0, v22, v13
	v_bfi_b32 v3, s0, v23, v14
	v_bfi_b32 v11, s0, v24, v15
	v_pack_b32_f16 v3, v3, v11
	v_pack_b32_f16 v2, v2, v10
	v_pack_b32_f16 v1, v1, v9
	v_pack_b32_f16 v0, v0, v8
	v_bfi_b32 v17, s0, v17, v20
	v_bfi_b32 v26, s0, v21, v32
	v_bfi_b32 v27, s0, v33, v34
	v_bfi_b32 v28, s0, v35, v66
	v_bfi_b32 v4, s0, v4, v67
	v_bfi_b32 v29, s0, v5, v68
	v_bfi_b32 v7, s0, v7, v25
	v_pack_b32_f16 v4, v4, v29
	v_cvt_f16_f32_e32 v16, v16
	s_nop 0
	v_mfma_f32_16x16x32_f16 v[12:15], v[220:223], v[0:3], 0
	v_bfi_b32 v5, s0, v16, v69
	v_lshlrev_b32_e32 v16, 2, v6
	s_nop 0
	v_mfma_f32_16x16x32_f16 v[8:11], v[212:215], v[0:3], 0
	v_pack_b32_f16 v5, v5, v7
	s_nop 0
	v_mfma_f32_16x16x32_f16 v[18:21], v[228:231], v[0:3], 0
	s_nop 0
	v_mfma_f32_16x16x32_f16 v[22:25], v[236:239], v[0:3], 0
	v_pack_b32_f16 v3, v27, v28
	v_pack_b32_f16 v2, v17, v26
	s_nop 0
	s_nop 0
	s_nop 0
	s_nop 0
	s_nop 0
	v_mfma_f32_16x16x32_f16 v[8:11], v[216:219], v[2:5], v[8:11]
	s_nop 0
	v_mfma_f32_16x16x32_f16 v[12:15], v[224:227], v[2:5], v[12:15]
	s_nop 0
	v_mfma_f32_16x16x32_f16 v[18:21], v[232:235], v[2:5], v[18:21]
	s_nop 0
	s_nop 2
	v_pk_add_f32 v[0:1], v[8:9], v[184:185]
	s_nop 0
	v_mfma_f32_16x16x32_f16 v[22:25], v[240:243], v[2:5], v[22:25]
	v_add_f32_e64 v2, v10, v186
	v_add_f32_e64 v3, v11, v187
	s_nop 0
	v_pk_add_f32 v[4:5], v[12:13], v[188:189]
	v_pk_add_f32 v[6:7], v[14:15], v[190:191]
	s_nop 0
	v_pk_add_f32 v[8:9], v[18:19], v[192:193]
	v_pk_add_f32 v[10:11], v[20:21], v[194:195]
	s_nop 0
	v_pk_add_f32 v[12:13], v[22:23], v[196:197]
	v_pk_add_f32 v[14:15], v[24:25], v[198:199]
	s_and_saveexec_b64 s[0:1], s[8:9]
	s_cbranch_execz .LBB2_182
	v_mov_b32_e32 v109, 0
	v_lshlrev_b64 v[18:19], 8, v[108:109]
	v_lshl_add_u64 v[18:19], s[22:23], 0, v[18:19]
	v_mov_b32_e32 v17, v109
	v_lshl_add_u64 v[18:19], v[18:19], 0, v[16:17]
	global_store_dwordx4 v[18:19], v[0:3], off
	global_store_dwordx4 v[18:19], v[4:7], off offset:64
	global_store_dwordx4 v[18:19], v[8:11], off offset:128
	global_store_dwordx4 v[18:19], v[12:15], off offset:192
